# MoE epilogue VALU peepholes: P10 x16 scale folded into the routing weight (bit-identical), first-row-group weight load joins the batched loads; P9 two constant multiplies before exp fused into one
# speedup vs baseline: 1.0228x; 1.0076x over previous
.LBB0_1160:
	v_lshl_or_b32 v148, s65, 8, v161
	v_ashrrev_i32_e32 v149, 31, v148
	s_nop 15
	s_nop 15
	v_add_u32_e32 v144, s39, v160
	v_cmp_gt_i32_e32 vcc, s38, v160
	v_ashrrev_i32_e32 v150, 1, v148
	v_cndmask_b32_e32 v144, -1, v144, vcc
	v_cmp_lt_i32_e32 vcc, -1, v144
	v_ashrrev_i32_e32 v151, 31, v150
	s_and_saveexec_b64 s[10:11], vcc
	s_cbranch_execz .LBB0_1162
	v_pk_fma_f32 v[124:125], v[124:125], s[20:21], v[232:233] op_sel_hi:[1,0,1]
	v_lshlrev_b64 v[176:177], 11, v[144:145]
	v_min_f32_e32 v124, 0x40e00000, v124
	v_mul_f32_e32 v144, 0xc01d265f, v124
	v_exp_f32_e32 v144, v144
	v_pk_fma_f32 v[126:127], v[126:127], s[20:21], v[234:235] op_sel_hi:[1,0,1]
	v_pk_fma_f32 v[120:121], v[120:121], s[20:21], v[236:237] op_sel_hi:[1,0,1]
	v_min_f32_e32 v126, 0x40e00000, v126
	v_add_f32_e32 v144, 1.0, v144
	v_mul_f32_e32 v149, 0xc01d265f, v126
	v_rcp_f32_e32 v144, v144
	v_exp_f32_e32 v149, v149
	v_med3_f32 v125, v125, s61, v172
	v_mul_f32_e32 v124, v124, v144
	v_add_f32_e32 v125, 1.0, v125
	v_min_f32_e32 v120, 0x40e00000, v120
	v_add_f32_e32 v144, 1.0, v149
	v_mul_f32_e32 v124, v125, v124
	v_med3_f32 v125, v127, s61, v172
	v_mul_f32_e32 v127, 0xc01d265f, v120
	v_rcp_f32_e32 v144, v144
	v_exp_f32_e32 v127, v127
	v_pk_fma_f32 v[122:123], v[122:123], s[20:21], v[238:239] op_sel_hi:[1,0,1]
	v_mul_f32_e32 v126, v126, v144
	v_add_f32_e32 v125, 1.0, v125
	v_min_f32_e32 v122, 0x40e00000, v122
	v_mul_f32_e32 v125, v125, v126
	v_add_f32_e32 v126, 1.0, v127
	v_mul_f32_e32 v127, 0xc01d265f, v122
	v_rcp_f32_e32 v126, v126
	v_exp_f32_e32 v127, v127
	v_med3_f32 v121, v121, s61, v172
	v_mul_f32_e32 v120, v120, v126
	v_add_f32_e32 v121, 1.0, v121
	v_mul_f32_e32 v120, v121, v120
	v_add_f32_e32 v121, 1.0, v127
	v_rcp_f32_e32 v121, v121
	v_cvt_pk_fp8_f32 v200, v124, v125
	v_med3_f32 v123, v123, s61, v172
	v_mul_f32_e32 v121, v122, v121
	v_add_f32_e32 v122, 1.0, v123
	v_pk_fma_f32 v[116:117], v[116:117], s[20:21], v[240:241] op_sel_hi:[1,0,1]
	v_mul_f32_e32 v121, v122, v121
	v_min_f32_e32 v116, 0x40e00000, v116
	v_cvt_pk_fp8_f32 v200, v120, v121 op_sel:[0,0,1]
	v_mul_f32_e32 v120, 0xc01d265f, v116
	v_exp_f32_e32 v122, v120
	v_pk_fma_f32 v[118:119], v[118:119], s[20:21], v[242:243] op_sel_hi:[1,0,1]
	v_pk_fma_f32 v[112:113], v[112:113], s[20:21], v[244:245] op_sel_hi:[1,0,1]
	v_min_f32_e32 v118, 0x40e00000, v118
	v_add_f32_e32 v122, 1.0, v122
	v_mul_f32_e32 v123, 0xc01d265f, v118
	v_rcp_f32_e32 v122, v122
	v_exp_f32_e32 v123, v123
	v_med3_f32 v117, v117, s61, v172
	v_mul_f32_e32 v116, v116, v122
	v_add_f32_e32 v117, 1.0, v117
	v_min_f32_e32 v112, 0x40e00000, v112
	v_add_f32_e32 v122, 1.0, v123
	v_mul_f32_e32 v116, v117, v116
	v_med3_f32 v117, v119, s61, v172
	v_mul_f32_e32 v119, 0xc01d265f, v112
	v_rcp_f32_e32 v122, v122
	v_exp_f32_e32 v119, v119
	v_pk_fma_f32 v[114:115], v[114:115], s[20:21], v[246:247] op_sel_hi:[1,0,1]
	v_mul_f32_e32 v118, v118, v122
	v_add_f32_e32 v117, 1.0, v117
	v_min_f32_e32 v114, 0x40e00000, v114
	v_mul_f32_e32 v117, v117, v118
	v_add_f32_e32 v118, 1.0, v119
	v_mul_f32_e32 v119, 0xc01d265f, v114
	v_rcp_f32_e32 v118, v118
	v_exp_f32_e32 v119, v119
	v_med3_f32 v113, v113, s61, v172
	v_mul_f32_e32 v112, v112, v118
	v_add_f32_e32 v113, 1.0, v113
	v_mul_f32_e32 v112, v113, v112
	v_add_f32_e32 v113, 1.0, v119
	v_rcp_f32_e32 v113, v113
	v_cvt_pk_fp8_f32 v201, v116, v117
	v_med3_f32 v115, v115, s61, v172
	v_mul_f32_e32 v113, v114, v113
	v_add_f32_e32 v114, 1.0, v115
	v_mul_f32_e32 v113, v114, v113
	v_cvt_pk_fp8_f32 v201, v112, v113 op_sel:[0,0,1]
	v_lshl_add_u64 v[176:177], s[16:17], 0, v[176:177]
	v_lshl_add_u64 v[120:121], v[176:177], 0, v[150:151]
	global_store_dwordx2 v[120:121], v[200:201], off
.LBB0_1162:
	s_or_b64 exec, exec, s[10:11]
	v_add_u32_e32 v112, s39, v162
	v_cmp_gt_i32_e32 vcc, s38, v162
	s_nop 1
	v_cndmask_b32_e32 v144, -1, v112, vcc
	v_cmp_lt_i32_e32 vcc, -1, v144
	s_and_saveexec_b64 s[10:11], vcc
	s_cbranch_execz .LBB0_1164
	v_pk_fma_f32 v[108:109], v[108:109], s[20:21], v[232:233] op_sel_hi:[1,0,1]
	v_pk_fma_f32 v[110:111], v[110:111], s[20:21], v[234:235] op_sel_hi:[1,0,1]
	v_min_f32_e32 v108, 0x40e00000, v108
	v_mul_f32_e32 v114, 0xc01d265f, v108
	v_exp_f32_e32 v114, v114
	v_min_f32_e32 v110, 0x40e00000, v110
	v_mul_f32_e32 v115, 0xc01d265f, v110
	v_add_f32_e32 v114, 1.0, v114
	v_rcp_f32_e32 v114, v114
	v_exp_f32_e32 v115, v115
	v_pk_fma_f32 v[104:105], v[104:105], s[20:21], v[236:237] op_sel_hi:[1,0,1]
	v_med3_f32 v109, v109, s61, v172
	v_mul_f32_e32 v108, v108, v114
	v_add_f32_e32 v109, 1.0, v109
	v_min_f32_e32 v104, 0x40e00000, v104
	v_add_f32_e32 v114, 1.0, v115
	v_mul_f32_e32 v108, v109, v108
	v_med3_f32 v109, v111, s61, v172
	v_mul_f32_e32 v111, 0xc01d265f, v104
	v_rcp_f32_e32 v114, v114
	v_exp_f32_e32 v111, v111
	v_pk_fma_f32 v[106:107], v[106:107], s[20:21], v[238:239] op_sel_hi:[1,0,1]
	v_mul_f32_e32 v110, v110, v114
	v_add_f32_e32 v109, 1.0, v109
	v_min_f32_e32 v106, 0x40e00000, v106
	v_mul_f32_e32 v109, v109, v110
	v_add_f32_e32 v110, 1.0, v111
	v_mul_f32_e32 v111, 0xc01d265f, v106
	v_rcp_f32_e32 v110, v110
	v_exp_f32_e32 v111, v111
	v_med3_f32 v105, v105, s61, v172
	v_mul_f32_e32 v104, v104, v110
	v_add_f32_e32 v105, 1.0, v105
	v_mul_f32_e32 v104, v105, v104
	v_add_f32_e32 v105, 1.0, v111
	v_rcp_f32_e32 v105, v105
	v_cvt_pk_fp8_f32 v202, v108, v109
	v_med3_f32 v107, v107, s61, v172
	v_mul_f32_e32 v105, v106, v105
	v_add_f32_e32 v106, 1.0, v107
	v_pk_fma_f32 v[100:101], v[100:101], s[20:21], v[240:241] op_sel_hi:[1,0,1]
	v_mul_f32_e32 v105, v106, v105
	v_min_f32_e32 v100, 0x40e00000, v100
	v_cvt_pk_fp8_f32 v202, v104, v105 op_sel:[0,0,1]
	v_mul_f32_e32 v104, 0xc01d265f, v100
	v_exp_f32_e32 v106, v104
	v_pk_fma_f32 v[102:103], v[102:103], s[20:21], v[242:243] op_sel_hi:[1,0,1]
	v_pk_fma_f32 v[96:97], v[96:97], s[20:21], v[244:245] op_sel_hi:[1,0,1]
	v_min_f32_e32 v102, 0x40e00000, v102
	v_add_f32_e32 v106, 1.0, v106
	v_mul_f32_e32 v107, 0xc01d265f, v102
	v_rcp_f32_e32 v106, v106
	v_exp_f32_e32 v107, v107
	v_med3_f32 v101, v101, s61, v172
	v_mul_f32_e32 v100, v100, v106
	v_add_f32_e32 v101, 1.0, v101
	v_min_f32_e32 v96, 0x40e00000, v96
	v_add_f32_e32 v106, 1.0, v107
	v_mul_f32_e32 v100, v101, v100
	v_med3_f32 v101, v103, s61, v172
	v_mul_f32_e32 v103, 0xc01d265f, v96
	v_rcp_f32_e32 v106, v106
	v_exp_f32_e32 v103, v103
	v_pk_fma_f32 v[98:99], v[98:99], s[20:21], v[246:247] op_sel_hi:[1,0,1]
	v_mul_f32_e32 v102, v102, v106
	v_add_f32_e32 v101, 1.0, v101
	v_min_f32_e32 v98, 0x40e00000, v98
	v_mul_f32_e32 v101, v101, v102
	v_add_f32_e32 v102, 1.0, v103
	v_mul_f32_e32 v103, 0xc01d265f, v98
	v_rcp_f32_e32 v102, v102
	v_exp_f32_e32 v103, v103
	v_med3_f32 v97, v97, s61, v172
	v_mul_f32_e32 v96, v96, v102
	v_add_f32_e32 v97, 1.0, v97
	v_mul_f32_e32 v96, v97, v96
	v_add_f32_e32 v97, 1.0, v103
	v_rcp_f32_e32 v97, v97
	v_cvt_pk_fp8_f32 v203, v100, v101
	v_med3_f32 v99, v99, s61, v172
	v_mul_f32_e32 v97, v98, v97
	v_add_f32_e32 v98, 1.0, v99
	v_mul_f32_e32 v97, v98, v97
	v_cvt_pk_fp8_f32 v203, v96, v97 op_sel:[0,0,1]
	v_lshlrev_b64 v[112:113], 11, v[144:145]
	v_lshl_add_u64 v[112:113], s[16:17], 0, v[112:113]
	v_lshl_add_u64 v[104:105], v[112:113], 0, v[150:151]
	global_store_dwordx2 v[104:105], v[202:203], off
.LBB0_1164:
	s_or_b64 exec, exec, s[10:11]
	v_add_u32_e32 v96, s39, v163
	v_cmp_gt_i32_e32 vcc, s38, v163
	s_nop 1
	v_cndmask_b32_e32 v144, -1, v96, vcc
	v_cmp_lt_i32_e32 vcc, -1, v144
	s_and_saveexec_b64 s[10:11], vcc
	s_cbranch_execz .LBB0_1166
	v_pk_fma_f32 v[92:93], v[92:93], s[20:21], v[232:233] op_sel_hi:[1,0,1]
	v_pk_fma_f32 v[94:95], v[94:95], s[20:21], v[234:235] op_sel_hi:[1,0,1]
	v_min_f32_e32 v92, 0x40e00000, v92
	v_mul_f32_e32 v98, 0xc01d265f, v92
	v_exp_f32_e32 v98, v98
	v_min_f32_e32 v94, 0x40e00000, v94
	v_mul_f32_e32 v99, 0xc01d265f, v94
	v_add_f32_e32 v98, 1.0, v98
	v_rcp_f32_e32 v98, v98
	v_exp_f32_e32 v99, v99
	v_pk_fma_f32 v[88:89], v[88:89], s[20:21], v[236:237] op_sel_hi:[1,0,1]
	v_med3_f32 v93, v93, s61, v172
	v_mul_f32_e32 v92, v92, v98
	v_add_f32_e32 v93, 1.0, v93
	v_min_f32_e32 v88, 0x40e00000, v88
	v_add_f32_e32 v98, 1.0, v99
	v_mul_f32_e32 v92, v93, v92
	v_med3_f32 v93, v95, s61, v172
	v_mul_f32_e32 v95, 0xc01d265f, v88
	v_rcp_f32_e32 v98, v98
	v_exp_f32_e32 v95, v95
	v_pk_fma_f32 v[90:91], v[90:91], s[20:21], v[238:239] op_sel_hi:[1,0,1]
	v_mul_f32_e32 v94, v94, v98
	v_add_f32_e32 v93, 1.0, v93
	v_min_f32_e32 v90, 0x40e00000, v90
	v_mul_f32_e32 v93, v93, v94
	v_add_f32_e32 v94, 1.0, v95
	v_mul_f32_e32 v95, 0xc01d265f, v90
	v_rcp_f32_e32 v94, v94
	v_exp_f32_e32 v95, v95
	v_med3_f32 v89, v89, s61, v172
	v_mul_f32_e32 v88, v88, v94
	v_add_f32_e32 v89, 1.0, v89
	v_mul_f32_e32 v88, v89, v88
	v_add_f32_e32 v89, 1.0, v95
	v_rcp_f32_e32 v89, v89
	v_cvt_pk_fp8_f32 v204, v92, v93
	v_med3_f32 v91, v91, s61, v172
	v_mul_f32_e32 v89, v90, v89
	v_add_f32_e32 v90, 1.0, v91
	v_pk_fma_f32 v[84:85], v[84:85], s[20:21], v[240:241] op_sel_hi:[1,0,1]
	v_mul_f32_e32 v89, v90, v89
	v_min_f32_e32 v84, 0x40e00000, v84
	v_cvt_pk_fp8_f32 v204, v88, v89 op_sel:[0,0,1]
	v_mul_f32_e32 v88, 0xc01d265f, v84
	v_exp_f32_e32 v90, v88
	v_pk_fma_f32 v[86:87], v[86:87], s[20:21], v[242:243] op_sel_hi:[1,0,1]
	v_pk_fma_f32 v[80:81], v[80:81], s[20:21], v[244:245] op_sel_hi:[1,0,1]
	v_min_f32_e32 v86, 0x40e00000, v86
	v_add_f32_e32 v90, 1.0, v90
	v_mul_f32_e32 v91, 0xc01d265f, v86
	v_rcp_f32_e32 v90, v90
	v_exp_f32_e32 v91, v91
	v_med3_f32 v85, v85, s61, v172
	v_mul_f32_e32 v84, v84, v90
	v_add_f32_e32 v85, 1.0, v85
	v_min_f32_e32 v80, 0x40e00000, v80
	v_add_f32_e32 v90, 1.0, v91
	v_mul_f32_e32 v84, v85, v84
	v_med3_f32 v85, v87, s61, v172
	v_mul_f32_e32 v87, 0xc01d265f, v80
	v_rcp_f32_e32 v90, v90
	v_exp_f32_e32 v87, v87
	v_pk_fma_f32 v[82:83], v[82:83], s[20:21], v[246:247] op_sel_hi:[1,0,1]
	v_mul_f32_e32 v86, v86, v90
	v_add_f32_e32 v85, 1.0, v85
	v_min_f32_e32 v82, 0x40e00000, v82
	v_mul_f32_e32 v85, v85, v86
	v_add_f32_e32 v86, 1.0, v87
	v_mul_f32_e32 v87, 0xc01d265f, v82
	v_rcp_f32_e32 v86, v86
	v_exp_f32_e32 v87, v87
	v_med3_f32 v81, v81, s61, v172
	v_mul_f32_e32 v80, v80, v86
	v_add_f32_e32 v81, 1.0, v81
	v_mul_f32_e32 v80, v81, v80
	v_add_f32_e32 v81, 1.0, v87
	v_rcp_f32_e32 v81, v81
	v_cvt_pk_fp8_f32 v205, v84, v85
	v_med3_f32 v83, v83, s61, v172
	v_mul_f32_e32 v81, v82, v81
	v_add_f32_e32 v82, 1.0, v83
	v_mul_f32_e32 v81, v82, v81
	v_cvt_pk_fp8_f32 v205, v80, v81 op_sel:[0,0,1]
	v_lshlrev_b64 v[96:97], 11, v[144:145]
	v_lshl_add_u64 v[96:97], s[16:17], 0, v[96:97]
	v_lshl_add_u64 v[88:89], v[96:97], 0, v[150:151]
	global_store_dwordx2 v[88:89], v[204:205], off
.LBB0_1166:
	s_or_b64 exec, exec, s[10:11]
	v_add_u32_e32 v80, s39, v164
	v_cmp_gt_i32_e32 vcc, s38, v164
	s_nop 1
	v_cndmask_b32_e32 v144, -1, v80, vcc
	v_cmp_lt_i32_e32 vcc, -1, v144
	s_and_saveexec_b64 s[10:11], vcc
	s_cbranch_execz .LBB0_1168
	v_pk_fma_f32 v[76:77], v[76:77], s[20:21], v[232:233] op_sel_hi:[1,0,1]
	v_pk_fma_f32 v[78:79], v[78:79], s[20:21], v[234:235] op_sel_hi:[1,0,1]
	v_min_f32_e32 v76, 0x40e00000, v76
	v_mul_f32_e32 v82, 0xc01d265f, v76
	v_exp_f32_e32 v82, v82
	v_min_f32_e32 v78, 0x40e00000, v78
	v_mul_f32_e32 v83, 0xc01d265f, v78
	v_add_f32_e32 v82, 1.0, v82
	v_rcp_f32_e32 v82, v82
	v_exp_f32_e32 v83, v83
	v_pk_fma_f32 v[72:73], v[72:73], s[20:21], v[236:237] op_sel_hi:[1,0,1]
	v_med3_f32 v77, v77, s61, v172
	v_mul_f32_e32 v76, v76, v82
	v_add_f32_e32 v77, 1.0, v77
	v_min_f32_e32 v72, 0x40e00000, v72
	v_add_f32_e32 v82, 1.0, v83
	v_mul_f32_e32 v76, v77, v76
	v_med3_f32 v77, v79, s61, v172
	v_mul_f32_e32 v79, 0xc01d265f, v72
	v_rcp_f32_e32 v82, v82
	v_exp_f32_e32 v79, v79
	v_pk_fma_f32 v[74:75], v[74:75], s[20:21], v[238:239] op_sel_hi:[1,0,1]
	v_mul_f32_e32 v78, v78, v82
	v_add_f32_e32 v77, 1.0, v77
	v_min_f32_e32 v74, 0x40e00000, v74
	v_mul_f32_e32 v77, v77, v78
	v_add_f32_e32 v78, 1.0, v79
	v_mul_f32_e32 v79, 0xc01d265f, v74
	v_rcp_f32_e32 v78, v78
	v_exp_f32_e32 v79, v79
	v_med3_f32 v73, v73, s61, v172
	v_mul_f32_e32 v72, v72, v78
	v_add_f32_e32 v73, 1.0, v73
	v_mul_f32_e32 v72, v73, v72
	v_add_f32_e32 v73, 1.0, v79
	v_rcp_f32_e32 v73, v73
	v_cvt_pk_fp8_f32 v206, v76, v77
	v_med3_f32 v75, v75, s61, v172
	v_mul_f32_e32 v73, v74, v73
	v_add_f32_e32 v74, 1.0, v75
	v_pk_fma_f32 v[68:69], v[68:69], s[20:21], v[240:241] op_sel_hi:[1,0,1]
	v_mul_f32_e32 v73, v74, v73
	v_min_f32_e32 v68, 0x40e00000, v68
	v_cvt_pk_fp8_f32 v206, v72, v73 op_sel:[0,0,1]
	v_mul_f32_e32 v72, 0xc01d265f, v68
	v_exp_f32_e32 v74, v72
	v_pk_fma_f32 v[70:71], v[70:71], s[20:21], v[242:243] op_sel_hi:[1,0,1]
	v_pk_fma_f32 v[64:65], v[64:65], s[20:21], v[244:245] op_sel_hi:[1,0,1]
	v_min_f32_e32 v70, 0x40e00000, v70
	v_add_f32_e32 v74, 1.0, v74
	v_mul_f32_e32 v75, 0xc01d265f, v70
	v_rcp_f32_e32 v74, v74
	v_exp_f32_e32 v75, v75
	v_med3_f32 v69, v69, s61, v172
	v_mul_f32_e32 v68, v68, v74
	v_add_f32_e32 v69, 1.0, v69
	v_min_f32_e32 v64, 0x40e00000, v64
	v_add_f32_e32 v74, 1.0, v75
	v_mul_f32_e32 v68, v69, v68
	v_med3_f32 v69, v71, s61, v172
	v_mul_f32_e32 v71, 0xc01d265f, v64
	v_rcp_f32_e32 v74, v74
	v_exp_f32_e32 v71, v71
	v_pk_fma_f32 v[66:67], v[66:67], s[20:21], v[246:247] op_sel_hi:[1,0,1]
	v_mul_f32_e32 v70, v70, v74
	v_add_f32_e32 v69, 1.0, v69
	v_min_f32_e32 v66, 0x40e00000, v66
	v_mul_f32_e32 v69, v69, v70
	v_add_f32_e32 v70, 1.0, v71
	v_mul_f32_e32 v71, 0xc01d265f, v66
	v_rcp_f32_e32 v70, v70
	v_exp_f32_e32 v71, v71
	v_med3_f32 v65, v65, s61, v172
	v_mul_f32_e32 v64, v64, v70
	v_add_f32_e32 v65, 1.0, v65
	v_mul_f32_e32 v64, v65, v64
	v_add_f32_e32 v65, 1.0, v71
	v_rcp_f32_e32 v65, v65
	v_cvt_pk_fp8_f32 v207, v68, v69
	v_med3_f32 v67, v67, s61, v172
	v_mul_f32_e32 v65, v66, v65
	v_add_f32_e32 v66, 1.0, v67
	v_mul_f32_e32 v65, v66, v65
	v_cvt_pk_fp8_f32 v207, v64, v65 op_sel:[0,0,1]
	v_lshlrev_b64 v[80:81], 11, v[144:145]
	v_lshl_add_u64 v[80:81], s[16:17], 0, v[80:81]
	v_lshl_add_u64 v[72:73], v[80:81], 0, v[150:151]
	global_store_dwordx2 v[72:73], v[206:207], off
.LBB0_1168:
	s_or_b64 exec, exec, s[10:11]
	v_add_u32_e32 v64, s39, v165
	v_cmp_gt_i32_e32 vcc, s38, v165
	s_nop 1
	v_cndmask_b32_e32 v144, -1, v64, vcc
	v_cmp_lt_i32_e32 vcc, -1, v144
	s_and_saveexec_b64 s[10:11], vcc
	s_cbranch_execz .LBB0_1170
	v_pk_fma_f32 v[60:61], v[60:61], s[20:21], v[232:233] op_sel_hi:[1,0,1]
	v_pk_fma_f32 v[62:63], v[62:63], s[20:21], v[234:235] op_sel_hi:[1,0,1]
	v_min_f32_e32 v60, 0x40e00000, v60
	v_mul_f32_e32 v66, 0xc01d265f, v60
	v_exp_f32_e32 v66, v66
	v_min_f32_e32 v62, 0x40e00000, v62
	v_mul_f32_e32 v67, 0xc01d265f, v62
	v_add_f32_e32 v66, 1.0, v66
	v_rcp_f32_e32 v66, v66
	v_exp_f32_e32 v67, v67
	v_pk_fma_f32 v[56:57], v[56:57], s[20:21], v[236:237] op_sel_hi:[1,0,1]
	v_med3_f32 v61, v61, s61, v172
	v_mul_f32_e32 v60, v60, v66
	v_add_f32_e32 v61, 1.0, v61
	v_min_f32_e32 v56, 0x40e00000, v56
	v_add_f32_e32 v66, 1.0, v67
	v_mul_f32_e32 v60, v61, v60
	v_med3_f32 v61, v63, s61, v172
	v_mul_f32_e32 v63, 0xc01d265f, v56
	v_rcp_f32_e32 v66, v66
	v_exp_f32_e32 v63, v63
	v_pk_fma_f32 v[58:59], v[58:59], s[20:21], v[238:239] op_sel_hi:[1,0,1]
	v_mul_f32_e32 v62, v62, v66
	v_add_f32_e32 v61, 1.0, v61
	v_min_f32_e32 v58, 0x40e00000, v58
	v_mul_f32_e32 v61, v61, v62
	v_add_f32_e32 v62, 1.0, v63
	v_mul_f32_e32 v63, 0xc01d265f, v58
	v_rcp_f32_e32 v62, v62
	v_exp_f32_e32 v63, v63
	v_med3_f32 v57, v57, s61, v172
	v_mul_f32_e32 v56, v56, v62
	v_add_f32_e32 v57, 1.0, v57
	v_mul_f32_e32 v56, v57, v56
	v_add_f32_e32 v57, 1.0, v63
	v_rcp_f32_e32 v57, v57
	v_cvt_pk_fp8_f32 v208, v60, v61
	v_med3_f32 v59, v59, s61, v172
	v_mul_f32_e32 v57, v58, v57
	v_add_f32_e32 v58, 1.0, v59
	v_pk_fma_f32 v[52:53], v[52:53], s[20:21], v[240:241] op_sel_hi:[1,0,1]
	v_mul_f32_e32 v57, v58, v57
	v_min_f32_e32 v52, 0x40e00000, v52
	v_cvt_pk_fp8_f32 v208, v56, v57 op_sel:[0,0,1]
	v_mul_f32_e32 v56, 0xc01d265f, v52
	v_exp_f32_e32 v58, v56
	v_pk_fma_f32 v[54:55], v[54:55], s[20:21], v[242:243] op_sel_hi:[1,0,1]
	v_pk_fma_f32 v[48:49], v[48:49], s[20:21], v[244:245] op_sel_hi:[1,0,1]
	v_min_f32_e32 v54, 0x40e00000, v54
	v_add_f32_e32 v58, 1.0, v58
	v_mul_f32_e32 v59, 0xc01d265f, v54
	v_rcp_f32_e32 v58, v58
	v_exp_f32_e32 v59, v59
	v_med3_f32 v53, v53, s61, v172
	v_mul_f32_e32 v52, v52, v58
	v_add_f32_e32 v53, 1.0, v53
	v_min_f32_e32 v48, 0x40e00000, v48
	v_add_f32_e32 v58, 1.0, v59
	v_mul_f32_e32 v52, v53, v52
	v_med3_f32 v53, v55, s61, v172
	v_mul_f32_e32 v55, 0xc01d265f, v48
	v_rcp_f32_e32 v58, v58
	v_exp_f32_e32 v55, v55
	v_pk_fma_f32 v[50:51], v[50:51], s[20:21], v[246:247] op_sel_hi:[1,0,1]
	v_mul_f32_e32 v54, v54, v58
	v_add_f32_e32 v53, 1.0, v53
	v_min_f32_e32 v50, 0x40e00000, v50
	v_mul_f32_e32 v53, v53, v54
	v_add_f32_e32 v54, 1.0, v55
	v_mul_f32_e32 v55, 0xc01d265f, v50
	v_rcp_f32_e32 v54, v54
	v_exp_f32_e32 v55, v55
	v_med3_f32 v49, v49, s61, v172
	v_mul_f32_e32 v48, v48, v54
	v_add_f32_e32 v49, 1.0, v49
	v_mul_f32_e32 v48, v49, v48
	v_add_f32_e32 v49, 1.0, v55
	v_rcp_f32_e32 v49, v49
	v_cvt_pk_fp8_f32 v209, v52, v53
	v_med3_f32 v51, v51, s61, v172
	v_mul_f32_e32 v49, v50, v49
	v_add_f32_e32 v50, 1.0, v51
	v_mul_f32_e32 v49, v50, v49
	v_cvt_pk_fp8_f32 v209, v48, v49 op_sel:[0,0,1]
	v_lshlrev_b64 v[64:65], 11, v[144:145]
	v_lshl_add_u64 v[64:65], s[16:17], 0, v[64:65]
	v_lshl_add_u64 v[56:57], v[64:65], 0, v[150:151]
	global_store_dwordx2 v[56:57], v[208:209], off
.LBB0_1170:
	s_or_b64 exec, exec, s[10:11]
	v_add_u32_e32 v48, s39, v166
	v_cmp_gt_i32_e32 vcc, s38, v166
	s_nop 1
	v_cndmask_b32_e32 v144, -1, v48, vcc
	v_cmp_lt_i32_e32 vcc, -1, v144
	s_and_saveexec_b64 s[10:11], vcc
	s_cbranch_execz .LBB0_1172
	v_pk_fma_f32 v[44:45], v[44:45], s[20:21], v[232:233] op_sel_hi:[1,0,1]
	v_pk_fma_f32 v[46:47], v[46:47], s[20:21], v[234:235] op_sel_hi:[1,0,1]
	v_min_f32_e32 v44, 0x40e00000, v44
	v_mul_f32_e32 v50, 0xc01d265f, v44
	v_exp_f32_e32 v50, v50
	v_min_f32_e32 v46, 0x40e00000, v46
	v_mul_f32_e32 v51, 0xc01d265f, v46
	v_add_f32_e32 v50, 1.0, v50
	v_rcp_f32_e32 v50, v50
	v_exp_f32_e32 v51, v51
	v_pk_fma_f32 v[40:41], v[40:41], s[20:21], v[236:237] op_sel_hi:[1,0,1]
	v_med3_f32 v45, v45, s61, v172
	v_mul_f32_e32 v44, v44, v50
	v_add_f32_e32 v45, 1.0, v45
	v_min_f32_e32 v40, 0x40e00000, v40
	v_add_f32_e32 v50, 1.0, v51
	v_mul_f32_e32 v44, v45, v44
	v_med3_f32 v45, v47, s61, v172
	v_mul_f32_e32 v47, 0xc01d265f, v40
	v_rcp_f32_e32 v50, v50
	v_exp_f32_e32 v47, v47
	v_pk_fma_f32 v[42:43], v[42:43], s[20:21], v[238:239] op_sel_hi:[1,0,1]
	v_mul_f32_e32 v46, v46, v50
	v_add_f32_e32 v45, 1.0, v45
	v_min_f32_e32 v42, 0x40e00000, v42
	v_mul_f32_e32 v45, v45, v46
	v_add_f32_e32 v46, 1.0, v47
	v_mul_f32_e32 v47, 0xc01d265f, v42
	v_rcp_f32_e32 v46, v46
	v_exp_f32_e32 v47, v47
	v_med3_f32 v41, v41, s61, v172
	v_mul_f32_e32 v40, v40, v46
	v_add_f32_e32 v41, 1.0, v41
	v_mul_f32_e32 v40, v41, v40
	v_add_f32_e32 v41, 1.0, v47
	v_rcp_f32_e32 v41, v41
	v_cvt_pk_fp8_f32 v210, v44, v45
	v_med3_f32 v43, v43, s61, v172
	v_mul_f32_e32 v41, v42, v41
	v_add_f32_e32 v42, 1.0, v43
	v_pk_fma_f32 v[36:37], v[36:37], s[20:21], v[240:241] op_sel_hi:[1,0,1]
	v_mul_f32_e32 v41, v42, v41
	v_min_f32_e32 v36, 0x40e00000, v36
	v_cvt_pk_fp8_f32 v210, v40, v41 op_sel:[0,0,1]
	v_mul_f32_e32 v40, 0xc01d265f, v36
	v_exp_f32_e32 v42, v40
	v_pk_fma_f32 v[38:39], v[38:39], s[20:21], v[242:243] op_sel_hi:[1,0,1]
	v_pk_fma_f32 v[32:33], v[32:33], s[20:21], v[244:245] op_sel_hi:[1,0,1]
	v_min_f32_e32 v38, 0x40e00000, v38
	v_add_f32_e32 v42, 1.0, v42
	v_mul_f32_e32 v43, 0xc01d265f, v38
	v_rcp_f32_e32 v42, v42
	v_exp_f32_e32 v43, v43
	v_med3_f32 v37, v37, s61, v172
	v_mul_f32_e32 v36, v36, v42
	v_add_f32_e32 v37, 1.0, v37
	v_min_f32_e32 v32, 0x40e00000, v32
	v_add_f32_e32 v42, 1.0, v43
	v_mul_f32_e32 v36, v37, v36
	v_med3_f32 v37, v39, s61, v172
	v_mul_f32_e32 v39, 0xc01d265f, v32
	v_rcp_f32_e32 v42, v42
	v_exp_f32_e32 v39, v39
	v_pk_fma_f32 v[34:35], v[34:35], s[20:21], v[246:247] op_sel_hi:[1,0,1]
	v_mul_f32_e32 v38, v38, v42
	v_add_f32_e32 v37, 1.0, v37
	v_min_f32_e32 v34, 0x40e00000, v34
	v_mul_f32_e32 v37, v37, v38
	v_add_f32_e32 v38, 1.0, v39
	v_mul_f32_e32 v39, 0xc01d265f, v34
	v_rcp_f32_e32 v38, v38
	v_exp_f32_e32 v39, v39
	v_med3_f32 v33, v33, s61, v172
	v_mul_f32_e32 v32, v32, v38
	v_add_f32_e32 v33, 1.0, v33
	v_mul_f32_e32 v32, v33, v32
	v_add_f32_e32 v33, 1.0, v39
	v_rcp_f32_e32 v33, v33
	v_cvt_pk_fp8_f32 v211, v36, v37
	v_med3_f32 v35, v35, s61, v172
	v_mul_f32_e32 v33, v34, v33
	v_add_f32_e32 v34, 1.0, v35
	v_mul_f32_e32 v33, v34, v33
	v_cvt_pk_fp8_f32 v211, v32, v33 op_sel:[0,0,1]
	v_lshlrev_b64 v[48:49], 11, v[144:145]
	v_lshl_add_u64 v[48:49], s[16:17], 0, v[48:49]
	v_lshl_add_u64 v[40:41], v[48:49], 0, v[150:151]
	global_store_dwordx2 v[40:41], v[210:211], off
.LBB0_1172:
	s_or_b64 exec, exec, s[10:11]
	v_add_u32_e32 v32, s39, v167
	v_cmp_gt_i32_e32 vcc, s38, v167
	s_nop 1
	v_cndmask_b32_e32 v144, -1, v32, vcc
	v_cmp_lt_i32_e32 vcc, -1, v144
	s_and_saveexec_b64 s[10:11], vcc
	s_cbranch_execz .LBB0_1174
	v_pk_fma_f32 v[28:29], v[28:29], s[20:21], v[232:233] op_sel_hi:[1,0,1]
	v_pk_fma_f32 v[30:31], v[30:31], s[20:21], v[234:235] op_sel_hi:[1,0,1]
	v_min_f32_e32 v28, 0x40e00000, v28
	v_mul_f32_e32 v34, 0xc01d265f, v28
	v_exp_f32_e32 v34, v34
	v_min_f32_e32 v30, 0x40e00000, v30
	v_mul_f32_e32 v35, 0xc01d265f, v30
	v_add_f32_e32 v34, 1.0, v34
	v_rcp_f32_e32 v34, v34
	v_exp_f32_e32 v35, v35
	v_pk_fma_f32 v[24:25], v[24:25], s[20:21], v[236:237] op_sel_hi:[1,0,1]
	v_med3_f32 v29, v29, s61, v172
	v_mul_f32_e32 v28, v28, v34
	v_add_f32_e32 v29, 1.0, v29
	v_min_f32_e32 v24, 0x40e00000, v24
	v_add_f32_e32 v34, 1.0, v35
	v_mul_f32_e32 v28, v29, v28
	v_med3_f32 v29, v31, s61, v172
	v_mul_f32_e32 v31, 0xc01d265f, v24
	v_rcp_f32_e32 v34, v34
	v_exp_f32_e32 v31, v31
	v_pk_fma_f32 v[26:27], v[26:27], s[20:21], v[238:239] op_sel_hi:[1,0,1]
	v_mul_f32_e32 v30, v30, v34
	v_add_f32_e32 v29, 1.0, v29
	v_min_f32_e32 v26, 0x40e00000, v26
	v_mul_f32_e32 v29, v29, v30
	v_add_f32_e32 v30, 1.0, v31
	v_mul_f32_e32 v31, 0xc01d265f, v26
	v_rcp_f32_e32 v30, v30
	v_exp_f32_e32 v31, v31
	v_med3_f32 v25, v25, s61, v172
	v_mul_f32_e32 v24, v24, v30
	v_add_f32_e32 v25, 1.0, v25
	v_mul_f32_e32 v24, v25, v24
	v_add_f32_e32 v25, 1.0, v31
	v_rcp_f32_e32 v25, v25
	v_cvt_pk_fp8_f32 v212, v28, v29
	v_med3_f32 v27, v27, s61, v172
	v_mul_f32_e32 v25, v26, v25
	v_add_f32_e32 v26, 1.0, v27
	v_pk_fma_f32 v[20:21], v[20:21], s[20:21], v[240:241] op_sel_hi:[1,0,1]
	v_mul_f32_e32 v25, v26, v25
	v_min_f32_e32 v20, 0x40e00000, v20
	v_cvt_pk_fp8_f32 v212, v24, v25 op_sel:[0,0,1]
	v_mul_f32_e32 v24, 0xc01d265f, v20
	v_exp_f32_e32 v26, v24
	v_pk_fma_f32 v[22:23], v[22:23], s[20:21], v[242:243] op_sel_hi:[1,0,1]
	v_pk_fma_f32 v[16:17], v[16:17], s[20:21], v[244:245] op_sel_hi:[1,0,1]
	v_min_f32_e32 v22, 0x40e00000, v22
	v_add_f32_e32 v26, 1.0, v26
	v_mul_f32_e32 v27, 0xc01d265f, v22
	v_rcp_f32_e32 v26, v26
	v_exp_f32_e32 v27, v27
	v_med3_f32 v21, v21, s61, v172
	v_mul_f32_e32 v20, v20, v26
	v_add_f32_e32 v21, 1.0, v21
	v_min_f32_e32 v16, 0x40e00000, v16
	v_add_f32_e32 v26, 1.0, v27
	v_mul_f32_e32 v20, v21, v20
	v_med3_f32 v21, v23, s61, v172
	v_mul_f32_e32 v23, 0xc01d265f, v16
	v_rcp_f32_e32 v26, v26
	v_exp_f32_e32 v23, v23
	v_pk_fma_f32 v[18:19], v[18:19], s[20:21], v[246:247] op_sel_hi:[1,0,1]
	v_mul_f32_e32 v22, v22, v26
	v_add_f32_e32 v21, 1.0, v21
	v_min_f32_e32 v18, 0x40e00000, v18
	v_mul_f32_e32 v21, v21, v22
	v_add_f32_e32 v22, 1.0, v23
	v_mul_f32_e32 v23, 0xc01d265f, v18
	v_rcp_f32_e32 v22, v22
	v_exp_f32_e32 v23, v23
	v_med3_f32 v17, v17, s61, v172
	v_mul_f32_e32 v16, v16, v22
	v_add_f32_e32 v17, 1.0, v17
	v_mul_f32_e32 v16, v17, v16
	v_add_f32_e32 v17, 1.0, v23
	v_rcp_f32_e32 v17, v17
	v_cvt_pk_fp8_f32 v213, v20, v21
	v_med3_f32 v19, v19, s61, v172
	v_mul_f32_e32 v17, v18, v17
	v_add_f32_e32 v18, 1.0, v19
	v_mul_f32_e32 v17, v18, v17
	v_cvt_pk_fp8_f32 v213, v16, v17 op_sel:[0,0,1]
	v_lshlrev_b64 v[32:33], 11, v[144:145]
	v_lshl_add_u64 v[32:33], s[16:17], 0, v[32:33]
	v_lshl_add_u64 v[24:25], v[32:33], 0, v[150:151]
	global_store_dwordx2 v[24:25], v[212:213], off
.LBB0_1174:
	s_or_b64 exec, exec, s[10:11]
	v_add_u32_e32 v16, s39, v168
	v_cmp_gt_i32_e32 vcc, s38, v168
	s_nop 1
	v_cndmask_b32_e32 v144, -1, v16, vcc
	v_cmp_lt_i32_e32 vcc, -1, v144
	s_and_saveexec_b64 s[10:11], vcc
	s_cbranch_execz .LBB0_1176
	v_pk_fma_f32 v[12:13], v[12:13], s[20:21], v[232:233] op_sel_hi:[1,0,1]
	v_pk_fma_f32 v[14:15], v[14:15], s[20:21], v[234:235] op_sel_hi:[1,0,1]
	v_min_f32_e32 v12, 0x40e00000, v12
	v_mul_f32_e32 v18, 0xc01d265f, v12
	v_exp_f32_e32 v18, v18
	v_min_f32_e32 v14, 0x40e00000, v14
	v_mul_f32_e32 v19, 0xc01d265f, v14
	v_add_f32_e32 v18, 1.0, v18
	v_rcp_f32_e32 v18, v18
	v_exp_f32_e32 v19, v19
	v_pk_fma_f32 v[8:9], v[8:9], s[20:21], v[236:237] op_sel_hi:[1,0,1]
	v_med3_f32 v13, v13, s61, v172
	v_mul_f32_e32 v12, v12, v18
	v_add_f32_e32 v13, 1.0, v13
	v_min_f32_e32 v8, 0x40e00000, v8
	v_add_f32_e32 v18, 1.0, v19
	v_mul_f32_e32 v12, v13, v12
	v_med3_f32 v13, v15, s61, v172
	v_mul_f32_e32 v15, 0xc01d265f, v8
	v_rcp_f32_e32 v18, v18
	v_exp_f32_e32 v15, v15
	v_pk_fma_f32 v[10:11], v[10:11], s[20:21], v[238:239] op_sel_hi:[1,0,1]
	v_mul_f32_e32 v14, v14, v18
	v_add_f32_e32 v13, 1.0, v13
	v_min_f32_e32 v10, 0x40e00000, v10
	v_mul_f32_e32 v13, v13, v14
	v_add_f32_e32 v14, 1.0, v15
	v_mul_f32_e32 v15, 0xc01d265f, v10
	v_rcp_f32_e32 v14, v14
	v_exp_f32_e32 v15, v15
	v_med3_f32 v9, v9, s61, v172
	v_mul_f32_e32 v8, v8, v14
	v_add_f32_e32 v9, 1.0, v9
	v_mul_f32_e32 v8, v9, v8
	v_add_f32_e32 v9, 1.0, v15
	v_rcp_f32_e32 v9, v9
	v_cvt_pk_fp8_f32 v214, v12, v13
	v_med3_f32 v11, v11, s61, v172
	v_mul_f32_e32 v9, v10, v9
	v_add_f32_e32 v10, 1.0, v11
	v_pk_fma_f32 v[4:5], v[4:5], s[20:21], v[240:241] op_sel_hi:[1,0,1]
	v_mul_f32_e32 v9, v10, v9
	v_min_f32_e32 v4, 0x40e00000, v4
	v_cvt_pk_fp8_f32 v214, v8, v9 op_sel:[0,0,1]
	v_mul_f32_e32 v8, 0xc01d265f, v4
	v_exp_f32_e32 v10, v8
	v_pk_fma_f32 v[6:7], v[6:7], s[20:21], v[242:243] op_sel_hi:[1,0,1]
	v_pk_fma_f32 v[0:1], v[0:1], s[20:21], v[244:245] op_sel_hi:[1,0,1]
	v_min_f32_e32 v6, 0x40e00000, v6
	v_add_f32_e32 v10, 1.0, v10
	v_mul_f32_e32 v11, 0xc01d265f, v6
	v_rcp_f32_e32 v10, v10
	v_exp_f32_e32 v11, v11
	v_med3_f32 v5, v5, s61, v172
	v_mul_f32_e32 v4, v4, v10
	v_add_f32_e32 v5, 1.0, v5
	v_min_f32_e32 v0, 0x40e00000, v0
	v_add_f32_e32 v10, 1.0, v11
	v_mul_f32_e32 v4, v5, v4
	v_med3_f32 v5, v7, s61, v172
	v_mul_f32_e32 v7, 0xc01d265f, v0
	v_rcp_f32_e32 v10, v10
	v_exp_f32_e32 v7, v7
	v_pk_fma_f32 v[2:3], v[2:3], s[20:21], v[246:247] op_sel_hi:[1,0,1]
	v_mul_f32_e32 v6, v6, v10
	v_add_f32_e32 v5, 1.0, v5
	v_min_f32_e32 v2, 0x40e00000, v2
	v_mul_f32_e32 v5, v5, v6
	v_add_f32_e32 v6, 1.0, v7
	v_mul_f32_e32 v7, 0xc01d265f, v2
	v_rcp_f32_e32 v6, v6
	v_exp_f32_e32 v7, v7
	v_med3_f32 v1, v1, s61, v172
	v_mul_f32_e32 v0, v0, v6
	v_add_f32_e32 v1, 1.0, v1
	v_mul_f32_e32 v0, v1, v0
	v_add_f32_e32 v1, 1.0, v7
	v_rcp_f32_e32 v1, v1
	v_cvt_pk_fp8_f32 v215, v4, v5
	v_med3_f32 v3, v3, s61, v172
	v_mul_f32_e32 v1, v2, v1
	v_add_f32_e32 v2, 1.0, v3
	v_mul_f32_e32 v1, v2, v1
	v_cvt_pk_fp8_f32 v215, v0, v1 op_sel:[0,0,1]
	v_lshlrev_b64 v[16:17], 11, v[144:145]
	v_lshl_add_u64 v[16:17], s[16:17], 0, v[16:17]
	v_lshl_add_u64 v[8:9], v[16:17], 0, v[150:151]
	global_store_dwordx2 v[8:9], v[214:215], off

.LBB0_1257:
	v_ashrrev_i32_e32 v147, 31, v146
	v_readlane_b32 s4, v253, 45
	v_lshlrev_b64 v[128:129], 13, v[146:147]
	v_readlane_b32 s16, v253, 57
	v_readlane_b32 s17, v253, 58
	v_readlane_b32 s14, v253, 55
	v_readlane_b32 s15, v253, 56
	v_lshl_add_u64 v[128:129], s[16:17], 0, v[128:129]
	v_cmp_gt_i32_e64 s[16:17], s81, v168
	v_readlane_b32 s12, v253, 53
	v_readlane_b32 s13, v253, 54
	v_cndmask_b32_e64 v144, 0, v168, s[16:17]
	v_cmp_gt_i32_e64 s[14:15], s81, v170
	v_readlane_b32 s10, v253, 51
	v_readlane_b32 s11, v253, 52
	v_lshlrev_b32_e32 v163, 2, v144
	v_cndmask_b32_e64 v144, 0, v170, s[14:15]
	v_cmp_gt_i32_e64 s[12:13], s81, v171
	v_readlane_b32 s8, v253, 49
	v_readlane_b32 s9, v253, 50
	v_lshlrev_b32_e32 v150, 2, v144
	v_cndmask_b32_e64 v144, 0, v171, s[12:13]
	v_cmp_gt_i32_e64 s[10:11], s81, v172
	v_lshl_or_b32 v148, s1, 8, v169
	s_ashr_i32 s1, s0, 31
	v_lshlrev_b64 v[164:165], 18, v[146:147]
	v_lshlrev_b32_e32 v152, 2, v144
	v_cndmask_b32_e64 v144, 0, v172, s[10:11]
	v_cmp_gt_i32_e64 s[8:9], s81, v173
	v_lshl_add_u64 v[146:147], s[34:35], 0, v[164:165]
	s_lshl_b64 s[0:1], s[0:1], 2
	v_lshlrev_b32_e32 v154, 2, v144
	v_cndmask_b32_e64 v144, 0, v173, s[8:9]
	v_readlane_b32 s5, v253, 46
	v_readlane_b32 s6, v253, 47
	v_readlane_b32 s7, v253, 48
	v_ashrrev_i32_e32 v149, 31, v148
	v_lshl_add_u64 v[146:147], v[146:147], 0, s[0:1]
	v_lshlrev_b64 v[192:193], 2, v[144:145]
	s_nop 15
	s_nop 15
	v_lshl_add_u64 v[132:133], v[148:149], 2, v[128:129]
	v_readfirstlane_b32 s4, v146
	v_readfirstlane_b32 s5, v147
	v_lshl_add_u64 v[186:187], v[146:147], 0, v[192:193]
	v_cmp_gt_i32_e64 s[6:7], s81, v174
	global_load_dwordx4 v[136:139], v[132:133], off offset:16
	global_load_dwordx4 v[140:143], v[132:133], off
	global_load_dwordx4 v[128:131], v[132:133], off offset:48
	s_nop 0
	global_load_dwordx4 v[132:135], v[132:133], off offset:32
	v_cndmask_b32_e64 v144, 0, v174, s[6:7]
	global_load_dword v162, v163, s[4:5]
	global_load_dword v191, v150, s[4:5]
	global_load_dword v190, v152, s[4:5]
	global_load_dword v188, v[186:187], off
	global_load_dword v189, v154, s[4:5]
	v_cmp_gt_i32_e64 s[4:5], s81, v175
	v_lshlrev_b64 v[194:195], 2, v[144:145]
	v_cmp_gt_i32_e32 vcc, s81, v176
	v_cndmask_b32_e64 v144, 0, v175, s[4:5]
	v_lshlrev_b64 v[196:197], 2, v[144:145]
	v_lshl_add_u64 v[186:187], v[146:147], 0, v[194:195]
	v_lshl_add_u64 v[198:199], v[146:147], 0, v[196:197]
	v_cndmask_b32_e32 v144, 0, v176, vcc
	v_lshl_add_u64 v[164:165], s[30:31], 0, v[164:165]
	global_load_dword v187, v[186:187], off
	v_lshl_add_u64 v[164:165], v[164:165], 0, s[0:1]
	global_load_dword v186, v[198:199], off
	v_lshlrev_b64 v[198:199], 2, v[144:145]
	v_lshl_add_u64 v[146:147], v[146:147], 0, v[198:199]
	v_readfirstlane_b32 s0, v164
	v_readfirstlane_b32 s1, v165
	v_lshl_add_u64 v[192:193], v[164:165], 0, v[192:193]
	global_load_dword v147, v[146:147], off
	s_nop 2
	global_load_dword v160, v150, s[0:1]
	global_load_dword v158, v152, s[0:1]
	global_load_dword v156, v154, s[0:1]
	v_readlane_b32 s18, v253, 59
	global_load_dword v154, v[192:193], off
	v_lshl_add_u64 v[192:193], v[164:165], 0, v[194:195]
	global_load_dword v152, v[192:193], off
	v_lshl_add_u64 v[192:193], v[164:165], 0, v[196:197]
	global_load_dword v150, v[192:193], off
	v_lshl_add_u64 v[192:193], v[164:165], 0, v[198:199]
	global_load_dword v146, v[192:193], off
	global_load_dword v242, v163, s[0:1]
	v_readlane_b32 s19, v253, 60
	s_waitcnt vmcnt(0)
	v_cndmask_b32_e64 v162, -1, v162, s[16:17]
	v_cmp_lt_i32_e64 s[0:1], -1, v162
	s_and_saveexec_b64 s[16:17], s[0:1]
	s_cbranch_execz .LBB0_1259
	v_mul_f32_e32 v242, 0x41800000, v242
	v_pk_fma_f32 v[124:125], v[124:125], s[40:41], v[140:141] op_sel_hi:[1,0,1]
	v_pk_fma_f32 v[120:121], v[120:121], s[40:41], v[136:137] op_sel_hi:[1,0,1]
	v_pk_fma_f32 v[116:117], v[116:117], s[40:41], v[132:133] op_sel_hi:[1,0,1]
	v_pk_fma_f32 v[112:113], v[112:113], s[40:41], v[128:129] op_sel_hi:[1,0,1]
	v_pk_fma_f32 v[126:127], v[126:127], s[40:41], v[142:143] op_sel_hi:[1,0,1]
	v_pk_fma_f32 v[122:123], v[122:123], s[40:41], v[138:139] op_sel_hi:[1,0,1]
	v_pk_fma_f32 v[118:119], v[118:119], s[40:41], v[134:135] op_sel_hi:[1,0,1]
	v_pk_fma_f32 v[114:115], v[114:115], s[40:41], v[130:131] op_sel_hi:[1,0,1]
	v_mov_b32_e32 v163, v145
	v_lshlrev_b64 v[162:163], 11, v[162:163]
	v_pk_mul_f32 v[124:125], v[124:125], v[242:243] op_sel_hi:[1,0]
	v_pk_mul_f32 v[120:121], v[120:121], v[242:243] op_sel_hi:[1,0]
	v_pk_mul_f32 v[116:117], v[116:117], v[242:243] op_sel_hi:[1,0]
	v_pk_mul_f32 v[112:113], v[112:113], v[242:243] op_sel_hi:[1,0]
	v_med3_f32 v124, v124, s75, v180
	v_med3_f32 v125, v125, s75, v180
	v_med3_f32 v120, v120, s75, v180
	v_med3_f32 v121, v121, s75, v180
	v_med3_f32 v116, v116, s75, v180
	v_med3_f32 v117, v117, s75, v180
	v_med3_f32 v112, v112, s75, v180
	v_med3_f32 v113, v113, s75, v180
	v_cvt_pk_fp8_f32 v200, v124, v125
	v_cvt_pk_fp8_f32 v201, v120, v121
	v_pk_mul_f32 v[126:127], v[126:127], v[242:243] op_sel_hi:[1,0]
	v_pk_mul_f32 v[122:123], v[122:123], v[242:243] op_sel_hi:[1,0]
	v_cvt_pk_fp8_f32 v202, v116, v117
	v_cvt_pk_fp8_f32 v203, v112, v113
	v_pk_mul_f32 v[118:119], v[118:119], v[242:243] op_sel_hi:[1,0]
	v_pk_mul_f32 v[114:115], v[114:115], v[242:243] op_sel_hi:[1,0]
	v_med3_f32 v126, v126, s75, v180
	v_med3_f32 v127, v127, s75, v180
	v_med3_f32 v122, v122, s75, v180
	v_med3_f32 v123, v123, s75, v180
	v_med3_f32 v118, v118, s75, v180
	v_med3_f32 v119, v119, s75, v180
	v_med3_f32 v114, v114, s75, v180
	v_med3_f32 v115, v115, s75, v180
	v_cvt_pk_fp8_f32 v200, v126, v127 op_sel:[0,0,1]
	v_cvt_pk_fp8_f32 v201, v122, v123 op_sel:[0,0,1]
	v_cvt_pk_fp8_f32 v202, v118, v119 op_sel:[0,0,1]
	v_cvt_pk_fp8_f32 v203, v114, v115 op_sel:[0,0,1]
	v_lshl_add_u64 v[112:113], s[36:37], 0, v[162:163]
	v_lshl_add_u64 v[112:113], v[112:113], 0, v[148:149]
	global_store_dwordx4 v[112:113], v[200:203], off
.LBB0_1259:
	s_or_b64 exec, exec, s[16:17]
	v_cndmask_b32_e64 v144, -1, v191, s[14:15]
	v_cmp_lt_i32_e64 s[0:1], -1, v144
	s_and_saveexec_b64 s[14:15], s[0:1]
	s_cbranch_execz .LBB0_1261
	v_mul_f32_e32 v160, 0x41800000, v160
	v_pk_fma_f32 v[108:109], v[108:109], s[40:41], v[140:141] op_sel_hi:[1,0,1]
	v_pk_fma_f32 v[110:111], v[110:111], s[40:41], v[142:143] op_sel_hi:[1,0,1]
	v_pk_mul_f32 v[108:109], v[108:109], v[160:161] op_sel_hi:[1,0]
	v_pk_mul_f32 v[110:111], v[110:111], v[160:161] op_sel_hi:[1,0]
	v_med3_f32 v114, v108, s75, v180
	v_med3_f32 v109, v109, s75, v180
	v_cvt_pk_fp8_f32 v204, v114, v109
	v_pk_fma_f32 v[104:105], v[104:105], s[40:41], v[136:137] op_sel_hi:[1,0,1]
	v_pk_mul_f32 v[104:105], v[104:105], v[160:161] op_sel_hi:[1,0]
	v_med3_f32 v110, v110, s75, v180
	v_med3_f32 v109, v111, s75, v180
	v_cvt_pk_fp8_f32 v204, v110, v109 op_sel:[0,0,1]
	v_med3_f32 v104, v104, s75, v180
	v_med3_f32 v105, v105, s75, v180
	v_pk_fma_f32 v[106:107], v[106:107], s[40:41], v[138:139] op_sel_hi:[1,0,1]
	v_cvt_pk_fp8_f32 v205, v104, v105
	v_pk_mul_f32 v[106:107], v[106:107], v[160:161] op_sel_hi:[1,0]
	v_pk_fma_f32 v[100:101], v[100:101], s[40:41], v[132:133] op_sel_hi:[1,0,1]
	v_pk_mul_f32 v[100:101], v[100:101], v[160:161] op_sel_hi:[1,0]
	v_med3_f32 v105, v106, s75, v180
	v_med3_f32 v104, v107, s75, v180
	v_cvt_pk_fp8_f32 v205, v105, v104 op_sel:[0,0,1]
	v_med3_f32 v104, v100, s75, v180
	v_med3_f32 v101, v101, s75, v180
	v_pk_fma_f32 v[102:103], v[102:103], s[40:41], v[134:135] op_sel_hi:[1,0,1]
	v_cvt_pk_fp8_f32 v206, v104, v101
	v_pk_mul_f32 v[102:103], v[102:103], v[160:161] op_sel_hi:[1,0]
	v_pk_fma_f32 v[96:97], v[96:97], s[40:41], v[128:129] op_sel_hi:[1,0,1]
	v_pk_mul_f32 v[96:97], v[96:97], v[160:161] op_sel_hi:[1,0]
	v_med3_f32 v102, v102, s75, v180
	v_med3_f32 v101, v103, s75, v180
	v_cvt_pk_fp8_f32 v206, v102, v101 op_sel:[0,0,1]
	v_med3_f32 v96, v96, s75, v180
	v_med3_f32 v97, v97, s75, v180
	v_pk_fma_f32 v[98:99], v[98:99], s[40:41], v[130:131] op_sel_hi:[1,0,1]
	v_cvt_pk_fp8_f32 v207, v96, v97
	v_pk_mul_f32 v[98:99], v[98:99], v[160:161] op_sel_hi:[1,0]
	v_lshlrev_b64 v[112:113], 11, v[144:145]
	v_med3_f32 v97, v98, s75, v180
	v_med3_f32 v96, v99, s75, v180
	v_cvt_pk_fp8_f32 v207, v97, v96 op_sel:[0,0,1]
	v_lshl_add_u64 v[96:97], s[36:37], 0, v[112:113]
	v_lshl_add_u64 v[96:97], v[96:97], 0, v[148:149]
	global_store_dwordx4 v[96:97], v[204:207], off
.LBB0_1261:
	s_or_b64 exec, exec, s[14:15]
	v_cndmask_b32_e64 v144, -1, v190, s[12:13]
	v_cmp_lt_i32_e64 s[0:1], -1, v144
	s_and_saveexec_b64 s[12:13], s[0:1]
	s_cbranch_execz .LBB0_1263
	v_mul_f32_e32 v158, 0x41800000, v158
	v_pk_fma_f32 v[92:93], v[92:93], s[40:41], v[140:141] op_sel_hi:[1,0,1]
	v_pk_fma_f32 v[94:95], v[94:95], s[40:41], v[142:143] op_sel_hi:[1,0,1]
	v_pk_mul_f32 v[92:93], v[92:93], v[158:159] op_sel_hi:[1,0]
	v_pk_mul_f32 v[94:95], v[94:95], v[158:159] op_sel_hi:[1,0]
	v_med3_f32 v98, v92, s75, v180
	v_med3_f32 v93, v93, s75, v180
	v_cvt_pk_fp8_f32 v208, v98, v93
	v_pk_fma_f32 v[88:89], v[88:89], s[40:41], v[136:137] op_sel_hi:[1,0,1]
	v_pk_mul_f32 v[88:89], v[88:89], v[158:159] op_sel_hi:[1,0]
	v_med3_f32 v94, v94, s75, v180
	v_med3_f32 v93, v95, s75, v180
	v_cvt_pk_fp8_f32 v208, v94, v93 op_sel:[0,0,1]
	v_med3_f32 v88, v88, s75, v180
	v_med3_f32 v89, v89, s75, v180
	v_pk_fma_f32 v[90:91], v[90:91], s[40:41], v[138:139] op_sel_hi:[1,0,1]
	v_cvt_pk_fp8_f32 v209, v88, v89
	v_pk_mul_f32 v[90:91], v[90:91], v[158:159] op_sel_hi:[1,0]
	v_pk_fma_f32 v[84:85], v[84:85], s[40:41], v[132:133] op_sel_hi:[1,0,1]
	v_pk_mul_f32 v[84:85], v[84:85], v[158:159] op_sel_hi:[1,0]
	v_med3_f32 v89, v90, s75, v180
	v_med3_f32 v88, v91, s75, v180
	v_cvt_pk_fp8_f32 v209, v89, v88 op_sel:[0,0,1]
	v_med3_f32 v88, v84, s75, v180
	v_med3_f32 v85, v85, s75, v180
	v_pk_fma_f32 v[86:87], v[86:87], s[40:41], v[134:135] op_sel_hi:[1,0,1]
	v_cvt_pk_fp8_f32 v210, v88, v85
	v_pk_mul_f32 v[86:87], v[86:87], v[158:159] op_sel_hi:[1,0]
	v_pk_fma_f32 v[80:81], v[80:81], s[40:41], v[128:129] op_sel_hi:[1,0,1]
	v_pk_mul_f32 v[80:81], v[80:81], v[158:159] op_sel_hi:[1,0]
	v_med3_f32 v86, v86, s75, v180
	v_med3_f32 v85, v87, s75, v180
	v_cvt_pk_fp8_f32 v210, v86, v85 op_sel:[0,0,1]
	v_med3_f32 v80, v80, s75, v180
	v_med3_f32 v81, v81, s75, v180
	v_pk_fma_f32 v[82:83], v[82:83], s[40:41], v[130:131] op_sel_hi:[1,0,1]
	v_cvt_pk_fp8_f32 v211, v80, v81
	v_pk_mul_f32 v[82:83], v[82:83], v[158:159] op_sel_hi:[1,0]
	v_lshlrev_b64 v[96:97], 11, v[144:145]
	v_med3_f32 v81, v82, s75, v180
	v_med3_f32 v80, v83, s75, v180
	v_cvt_pk_fp8_f32 v211, v81, v80 op_sel:[0,0,1]
	v_lshl_add_u64 v[80:81], s[36:37], 0, v[96:97]
	v_lshl_add_u64 v[80:81], v[80:81], 0, v[148:149]
	global_store_dwordx4 v[80:81], v[208:211], off
.LBB0_1263:
	s_or_b64 exec, exec, s[12:13]
	v_cndmask_b32_e64 v144, -1, v189, s[10:11]
	v_cmp_lt_i32_e64 s[0:1], -1, v144
	s_and_saveexec_b64 s[10:11], s[0:1]
	s_cbranch_execz .LBB0_1265
	v_mul_f32_e32 v156, 0x41800000, v156
	v_pk_fma_f32 v[76:77], v[76:77], s[40:41], v[140:141] op_sel_hi:[1,0,1]
	v_pk_fma_f32 v[78:79], v[78:79], s[40:41], v[142:143] op_sel_hi:[1,0,1]
	v_pk_mul_f32 v[76:77], v[76:77], v[156:157] op_sel_hi:[1,0]
	v_pk_mul_f32 v[78:79], v[78:79], v[156:157] op_sel_hi:[1,0]
	v_med3_f32 v82, v76, s75, v180
	v_med3_f32 v77, v77, s75, v180
	v_cvt_pk_fp8_f32 v212, v82, v77
	v_pk_fma_f32 v[72:73], v[72:73], s[40:41], v[136:137] op_sel_hi:[1,0,1]
	v_pk_mul_f32 v[72:73], v[72:73], v[156:157] op_sel_hi:[1,0]
	v_med3_f32 v78, v78, s75, v180
	v_med3_f32 v77, v79, s75, v180
	v_cvt_pk_fp8_f32 v212, v78, v77 op_sel:[0,0,1]
	v_med3_f32 v72, v72, s75, v180
	v_med3_f32 v73, v73, s75, v180
	v_pk_fma_f32 v[74:75], v[74:75], s[40:41], v[138:139] op_sel_hi:[1,0,1]
	v_cvt_pk_fp8_f32 v213, v72, v73
	v_pk_mul_f32 v[74:75], v[74:75], v[156:157] op_sel_hi:[1,0]
	v_pk_fma_f32 v[68:69], v[68:69], s[40:41], v[132:133] op_sel_hi:[1,0,1]
	v_pk_mul_f32 v[68:69], v[68:69], v[156:157] op_sel_hi:[1,0]
	v_med3_f32 v73, v74, s75, v180
	v_med3_f32 v72, v75, s75, v180
	v_cvt_pk_fp8_f32 v213, v73, v72 op_sel:[0,0,1]
	v_med3_f32 v72, v68, s75, v180
	v_med3_f32 v69, v69, s75, v180
	v_pk_fma_f32 v[70:71], v[70:71], s[40:41], v[134:135] op_sel_hi:[1,0,1]
	v_cvt_pk_fp8_f32 v214, v72, v69
	v_pk_mul_f32 v[70:71], v[70:71], v[156:157] op_sel_hi:[1,0]
	v_pk_fma_f32 v[64:65], v[64:65], s[40:41], v[128:129] op_sel_hi:[1,0,1]
	v_pk_mul_f32 v[64:65], v[64:65], v[156:157] op_sel_hi:[1,0]
	v_med3_f32 v70, v70, s75, v180
	v_med3_f32 v69, v71, s75, v180
	v_cvt_pk_fp8_f32 v214, v70, v69 op_sel:[0,0,1]
	v_med3_f32 v64, v64, s75, v180
	v_med3_f32 v65, v65, s75, v180
	v_pk_fma_f32 v[66:67], v[66:67], s[40:41], v[130:131] op_sel_hi:[1,0,1]
	v_cvt_pk_fp8_f32 v215, v64, v65
	v_pk_mul_f32 v[66:67], v[66:67], v[156:157] op_sel_hi:[1,0]
	v_lshlrev_b64 v[80:81], 11, v[144:145]
	v_med3_f32 v65, v66, s75, v180
	v_med3_f32 v64, v67, s75, v180
	v_cvt_pk_fp8_f32 v215, v65, v64 op_sel:[0,0,1]
	v_lshl_add_u64 v[64:65], s[36:37], 0, v[80:81]
	v_lshl_add_u64 v[64:65], v[64:65], 0, v[148:149]
	global_store_dwordx4 v[64:65], v[212:215], off
.LBB0_1265:
	s_or_b64 exec, exec, s[10:11]
	v_cndmask_b32_e64 v144, -1, v188, s[8:9]
	v_cmp_lt_i32_e64 s[0:1], -1, v144
	s_and_saveexec_b64 s[8:9], s[0:1]
	s_cbranch_execz .LBB0_1267
	v_mul_f32_e32 v154, 0x41800000, v154
	v_pk_fma_f32 v[60:61], v[60:61], s[40:41], v[140:141] op_sel_hi:[1,0,1]
	v_pk_fma_f32 v[62:63], v[62:63], s[40:41], v[142:143] op_sel_hi:[1,0,1]
	v_pk_mul_f32 v[60:61], v[60:61], v[154:155] op_sel_hi:[1,0]
	v_pk_mul_f32 v[62:63], v[62:63], v[154:155] op_sel_hi:[1,0]
	v_med3_f32 v66, v60, s75, v180
	v_med3_f32 v61, v61, s75, v180
	v_cvt_pk_fp8_f32 v216, v66, v61
	v_pk_fma_f32 v[56:57], v[56:57], s[40:41], v[136:137] op_sel_hi:[1,0,1]
	v_pk_mul_f32 v[56:57], v[56:57], v[154:155] op_sel_hi:[1,0]
	v_med3_f32 v62, v62, s75, v180
	v_med3_f32 v61, v63, s75, v180
	v_cvt_pk_fp8_f32 v216, v62, v61 op_sel:[0,0,1]
	v_med3_f32 v56, v56, s75, v180
	v_med3_f32 v57, v57, s75, v180
	v_pk_fma_f32 v[58:59], v[58:59], s[40:41], v[138:139] op_sel_hi:[1,0,1]
	v_cvt_pk_fp8_f32 v217, v56, v57
	v_pk_mul_f32 v[58:59], v[58:59], v[154:155] op_sel_hi:[1,0]
	v_pk_fma_f32 v[52:53], v[52:53], s[40:41], v[132:133] op_sel_hi:[1,0,1]
	v_pk_mul_f32 v[52:53], v[52:53], v[154:155] op_sel_hi:[1,0]
	v_med3_f32 v57, v58, s75, v180
	v_med3_f32 v56, v59, s75, v180
	v_cvt_pk_fp8_f32 v217, v57, v56 op_sel:[0,0,1]
	v_med3_f32 v56, v52, s75, v180
	v_med3_f32 v53, v53, s75, v180
	v_pk_fma_f32 v[54:55], v[54:55], s[40:41], v[134:135] op_sel_hi:[1,0,1]
	v_cvt_pk_fp8_f32 v218, v56, v53
	v_pk_mul_f32 v[54:55], v[54:55], v[154:155] op_sel_hi:[1,0]
	v_pk_fma_f32 v[48:49], v[48:49], s[40:41], v[128:129] op_sel_hi:[1,0,1]
	v_pk_mul_f32 v[48:49], v[48:49], v[154:155] op_sel_hi:[1,0]
	v_med3_f32 v54, v54, s75, v180
	v_med3_f32 v53, v55, s75, v180
	v_cvt_pk_fp8_f32 v218, v54, v53 op_sel:[0,0,1]
	v_med3_f32 v48, v48, s75, v180
	v_med3_f32 v49, v49, s75, v180
	v_pk_fma_f32 v[50:51], v[50:51], s[40:41], v[130:131] op_sel_hi:[1,0,1]
	v_cvt_pk_fp8_f32 v219, v48, v49
	v_pk_mul_f32 v[50:51], v[50:51], v[154:155] op_sel_hi:[1,0]
	v_lshlrev_b64 v[64:65], 11, v[144:145]
	v_med3_f32 v49, v50, s75, v180
	v_med3_f32 v48, v51, s75, v180
	v_cvt_pk_fp8_f32 v219, v49, v48 op_sel:[0,0,1]
	v_lshl_add_u64 v[48:49], s[36:37], 0, v[64:65]
	v_lshl_add_u64 v[48:49], v[48:49], 0, v[148:149]
	global_store_dwordx4 v[48:49], v[216:219], off
.LBB0_1267:
	s_or_b64 exec, exec, s[8:9]
	v_cndmask_b32_e64 v144, -1, v187, s[6:7]
	v_cmp_lt_i32_e64 s[0:1], -1, v144
	s_and_saveexec_b64 s[6:7], s[0:1]
	s_cbranch_execz .LBB0_1269
	v_mul_f32_e32 v152, 0x41800000, v152
	v_pk_fma_f32 v[44:45], v[44:45], s[40:41], v[140:141] op_sel_hi:[1,0,1]
	v_pk_fma_f32 v[46:47], v[46:47], s[40:41], v[142:143] op_sel_hi:[1,0,1]
	v_pk_mul_f32 v[44:45], v[44:45], v[152:153] op_sel_hi:[1,0]
	v_pk_mul_f32 v[46:47], v[46:47], v[152:153] op_sel_hi:[1,0]
	v_med3_f32 v50, v44, s75, v180
	v_med3_f32 v45, v45, s75, v180
	v_cvt_pk_fp8_f32 v220, v50, v45
	v_pk_fma_f32 v[40:41], v[40:41], s[40:41], v[136:137] op_sel_hi:[1,0,1]
	v_pk_mul_f32 v[40:41], v[40:41], v[152:153] op_sel_hi:[1,0]
	v_med3_f32 v46, v46, s75, v180
	v_med3_f32 v45, v47, s75, v180
	v_cvt_pk_fp8_f32 v220, v46, v45 op_sel:[0,0,1]
	v_med3_f32 v40, v40, s75, v180
	v_med3_f32 v41, v41, s75, v180
	v_pk_fma_f32 v[42:43], v[42:43], s[40:41], v[138:139] op_sel_hi:[1,0,1]
	v_cvt_pk_fp8_f32 v221, v40, v41
	v_pk_mul_f32 v[42:43], v[42:43], v[152:153] op_sel_hi:[1,0]
	v_pk_fma_f32 v[36:37], v[36:37], s[40:41], v[132:133] op_sel_hi:[1,0,1]
	v_pk_mul_f32 v[36:37], v[36:37], v[152:153] op_sel_hi:[1,0]
	v_med3_f32 v41, v42, s75, v180
	v_med3_f32 v40, v43, s75, v180
	v_cvt_pk_fp8_f32 v221, v41, v40 op_sel:[0,0,1]
	v_med3_f32 v40, v36, s75, v180
	v_med3_f32 v37, v37, s75, v180
	v_pk_fma_f32 v[38:39], v[38:39], s[40:41], v[134:135] op_sel_hi:[1,0,1]
	v_cvt_pk_fp8_f32 v222, v40, v37
	v_pk_mul_f32 v[38:39], v[38:39], v[152:153] op_sel_hi:[1,0]
	v_pk_fma_f32 v[32:33], v[32:33], s[40:41], v[128:129] op_sel_hi:[1,0,1]
	v_pk_mul_f32 v[32:33], v[32:33], v[152:153] op_sel_hi:[1,0]
	v_med3_f32 v38, v38, s75, v180
	v_med3_f32 v37, v39, s75, v180
	v_cvt_pk_fp8_f32 v222, v38, v37 op_sel:[0,0,1]
	v_med3_f32 v32, v32, s75, v180
	v_med3_f32 v33, v33, s75, v180
	v_pk_fma_f32 v[34:35], v[34:35], s[40:41], v[130:131] op_sel_hi:[1,0,1]
	v_cvt_pk_fp8_f32 v223, v32, v33
	v_pk_mul_f32 v[34:35], v[34:35], v[152:153] op_sel_hi:[1,0]
	v_lshlrev_b64 v[48:49], 11, v[144:145]
	v_med3_f32 v33, v34, s75, v180
	v_med3_f32 v32, v35, s75, v180
	v_cvt_pk_fp8_f32 v223, v33, v32 op_sel:[0,0,1]
	v_lshl_add_u64 v[32:33], s[36:37], 0, v[48:49]
	v_lshl_add_u64 v[32:33], v[32:33], 0, v[148:149]
	global_store_dwordx4 v[32:33], v[220:223], off
.LBB0_1269:
	s_or_b64 exec, exec, s[6:7]
	v_cndmask_b32_e64 v144, -1, v186, s[4:5]
	v_cmp_lt_i32_e64 s[0:1], -1, v144
	s_and_saveexec_b64 s[4:5], s[0:1]
	s_cbranch_execz .LBB0_1271
	v_mul_f32_e32 v150, 0x41800000, v150
	v_pk_fma_f32 v[28:29], v[28:29], s[40:41], v[140:141] op_sel_hi:[1,0,1]
	v_pk_fma_f32 v[30:31], v[30:31], s[40:41], v[142:143] op_sel_hi:[1,0,1]
	v_pk_mul_f32 v[28:29], v[28:29], v[150:151] op_sel_hi:[1,0]
	v_pk_mul_f32 v[30:31], v[30:31], v[150:151] op_sel_hi:[1,0]
	v_med3_f32 v34, v28, s75, v180
	v_med3_f32 v29, v29, s75, v180
	v_cvt_pk_fp8_f32 v224, v34, v29
	v_pk_fma_f32 v[24:25], v[24:25], s[40:41], v[136:137] op_sel_hi:[1,0,1]
	v_pk_mul_f32 v[24:25], v[24:25], v[150:151] op_sel_hi:[1,0]
	v_med3_f32 v30, v30, s75, v180
	v_med3_f32 v29, v31, s75, v180
	v_cvt_pk_fp8_f32 v224, v30, v29 op_sel:[0,0,1]
	v_med3_f32 v24, v24, s75, v180
	v_med3_f32 v25, v25, s75, v180
	v_pk_fma_f32 v[26:27], v[26:27], s[40:41], v[138:139] op_sel_hi:[1,0,1]
	v_cvt_pk_fp8_f32 v225, v24, v25
	v_pk_mul_f32 v[26:27], v[26:27], v[150:151] op_sel_hi:[1,0]
	v_pk_fma_f32 v[20:21], v[20:21], s[40:41], v[132:133] op_sel_hi:[1,0,1]
	v_pk_mul_f32 v[20:21], v[20:21], v[150:151] op_sel_hi:[1,0]
	v_med3_f32 v25, v26, s75, v180
	v_med3_f32 v24, v27, s75, v180
	v_cvt_pk_fp8_f32 v225, v25, v24 op_sel:[0,0,1]
	v_med3_f32 v24, v20, s75, v180
	v_med3_f32 v21, v21, s75, v180
	v_pk_fma_f32 v[22:23], v[22:23], s[40:41], v[134:135] op_sel_hi:[1,0,1]
	v_cvt_pk_fp8_f32 v226, v24, v21
	v_pk_mul_f32 v[22:23], v[22:23], v[150:151] op_sel_hi:[1,0]
	v_pk_fma_f32 v[16:17], v[16:17], s[40:41], v[128:129] op_sel_hi:[1,0,1]
	v_pk_mul_f32 v[16:17], v[16:17], v[150:151] op_sel_hi:[1,0]
	v_med3_f32 v22, v22, s75, v180
	v_med3_f32 v21, v23, s75, v180
	v_cvt_pk_fp8_f32 v226, v22, v21 op_sel:[0,0,1]
	v_med3_f32 v16, v16, s75, v180
	v_med3_f32 v17, v17, s75, v180
	v_pk_fma_f32 v[18:19], v[18:19], s[40:41], v[130:131] op_sel_hi:[1,0,1]
	v_cvt_pk_fp8_f32 v227, v16, v17
	v_pk_mul_f32 v[18:19], v[18:19], v[150:151] op_sel_hi:[1,0]
	v_lshlrev_b64 v[32:33], 11, v[144:145]
	v_med3_f32 v17, v18, s75, v180
	v_med3_f32 v16, v19, s75, v180
	v_cvt_pk_fp8_f32 v227, v17, v16 op_sel:[0,0,1]
	v_lshl_add_u64 v[16:17], s[36:37], 0, v[32:33]
	v_lshl_add_u64 v[16:17], v[16:17], 0, v[148:149]
	global_store_dwordx4 v[16:17], v[224:227], off
.LBB0_1271:
	s_or_b64 exec, exec, s[4:5]
	v_cndmask_b32_e32 v144, -1, v147, vcc
	v_cmp_lt_i32_e32 vcc, -1, v144
	s_and_saveexec_b64 s[0:1], vcc
	s_cbranch_execz .LBB0_1273
	v_mul_f32_e32 v146, 0x41800000, v146
	v_pk_fma_f32 v[12:13], v[12:13], s[40:41], v[140:141] op_sel_hi:[1,0,1]
	v_pk_fma_f32 v[14:15], v[14:15], s[40:41], v[142:143] op_sel_hi:[1,0,1]
	v_pk_mul_f32 v[12:13], v[12:13], v[146:147] op_sel_hi:[1,0]
	v_pk_mul_f32 v[14:15], v[14:15], v[146:147] op_sel_hi:[1,0]
	v_med3_f32 v18, v12, s75, v180
	v_med3_f32 v13, v13, s75, v180
	v_cvt_pk_fp8_f32 v228, v18, v13
	v_pk_fma_f32 v[8:9], v[8:9], s[40:41], v[136:137] op_sel_hi:[1,0,1]
	v_pk_mul_f32 v[8:9], v[8:9], v[146:147] op_sel_hi:[1,0]
	v_med3_f32 v14, v14, s75, v180
	v_med3_f32 v13, v15, s75, v180
	v_cvt_pk_fp8_f32 v228, v14, v13 op_sel:[0,0,1]
	v_med3_f32 v8, v8, s75, v180
	v_med3_f32 v9, v9, s75, v180
	v_pk_fma_f32 v[10:11], v[10:11], s[40:41], v[138:139] op_sel_hi:[1,0,1]
	v_cvt_pk_fp8_f32 v229, v8, v9
	v_pk_mul_f32 v[10:11], v[10:11], v[146:147] op_sel_hi:[1,0]
	v_pk_fma_f32 v[4:5], v[4:5], s[40:41], v[132:133] op_sel_hi:[1,0,1]
	v_pk_mul_f32 v[4:5], v[4:5], v[146:147] op_sel_hi:[1,0]
	v_med3_f32 v9, v10, s75, v180
	v_med3_f32 v8, v11, s75, v180
	v_cvt_pk_fp8_f32 v229, v9, v8 op_sel:[0,0,1]
	v_med3_f32 v8, v4, s75, v180
	v_med3_f32 v5, v5, s75, v180
	v_pk_fma_f32 v[6:7], v[6:7], s[40:41], v[134:135] op_sel_hi:[1,0,1]
	v_cvt_pk_fp8_f32 v230, v8, v5
	v_pk_mul_f32 v[6:7], v[6:7], v[146:147] op_sel_hi:[1,0]
	v_pk_fma_f32 v[0:1], v[0:1], s[40:41], v[128:129] op_sel_hi:[1,0,1]
	v_pk_mul_f32 v[0:1], v[0:1], v[146:147] op_sel_hi:[1,0]
	v_med3_f32 v6, v6, s75, v180
	v_med3_f32 v5, v7, s75, v180
	v_cvt_pk_fp8_f32 v230, v6, v5 op_sel:[0,0,1]
	v_med3_f32 v0, v0, s75, v180
	v_med3_f32 v1, v1, s75, v180
	v_pk_fma_f32 v[2:3], v[2:3], s[40:41], v[130:131] op_sel_hi:[1,0,1]
	v_cvt_pk_fp8_f32 v231, v0, v1
	v_pk_mul_f32 v[2:3], v[2:3], v[146:147] op_sel_hi:[1,0]
	v_lshlrev_b64 v[16:17], 11, v[144:145]
	v_med3_f32 v1, v2, s75, v180
	v_med3_f32 v0, v3, s75, v180
	v_cvt_pk_fp8_f32 v231, v1, v0 op_sel:[0,0,1]
	v_lshl_add_u64 v[0:1], s[36:37], 0, v[16:17]
	v_lshl_add_u64 v[0:1], v[0:1], 0, v[148:149]
	global_store_dwordx4 v[0:1], v[228:231], off
